# grid barrier: the agent-scope cache invalidate is issued when the workgroup arrives (after its arrival atomic returns) and completes while it waits, instead of after the release is observed; the waiti
# speedup vs baseline: 1.0068x; 1.0059x over previous
.LBB0_125:
	s_or_b64 exec, exec, s[6:7]
	v_cvt_f32_u32_e32 v5, v3
	s_waitcnt vmcnt(0)
	buffer_inv sc1
	v_readfirstlane_b32 s4, v4
	v_sub_u32_e32 v4, 0, v3
	v_rcp_iflag_f32_e32 v5, v5
	v_add_u32_e32 v6, s4, v2
	v_mul_f32_e32 v5, 0x4f7ffffe, v5
	v_cvt_u32_f32_e32 v5, v5
	v_mul_lo_u32 v2, v4, v5
	v_mul_hi_u32 v2, v5, v2
	v_add_u32_e32 v2, v5, v2
	v_mul_hi_u32 v2, v6, v2
	v_mul_lo_u32 v4, v2, v3
	v_sub_u32_e32 v4, v6, v4
	v_add_u32_e32 v5, 1, v2
	v_cmp_ge_u32_e32 vcc, v4, v3
	s_nop 1
	v_cndmask_b32_e32 v2, v2, v5, vcc
	v_sub_u32_e32 v5, v4, v3
	v_cndmask_b32_e32 v4, v4, v5, vcc
	v_add_u32_e32 v5, 1, v2
	v_cmp_ge_u32_e32 vcc, v4, v3
	v_add_u32_e32 v4, 1, v6
	s_nop 0
	v_cndmask_b32_e32 v2, v2, v5, vcc
	v_mul_lo_u32 v5, v3, v2
	v_add_u32_e32 v3, v5, v3
	v_cmp_ne_u32_e32 vcc, v4, v3
	s_and_saveexec_b64 s[4:5], vcc
	s_xor_b64 s[4:5], exec, s[4:5]
	s_cbranch_execz .LBB0_139
	s_movk_i32 s6, 0xd40
	s_mov_b32 s7, 0
	s_lshl_b64 s[6:7], s[6:7], 2
	s_add_u32 s8, s54, s6
	s_addc_u32 s9, s55, s7
	s_waitcnt lgkmcnt(0)
	v_mov_b32_e32 v1, 0
	global_load_dword v3, v1, s[8:9] sc1
	s_waitcnt vmcnt(0)
	v_cmp_eq_u32_e32 vcc, v3, v2
	s_and_saveexec_b64 s[6:7], vcc
	s_cbranch_execz .LBB0_138
	s_mov_b32 s20, 1
	s_mov_b64 s[10:11], 0
	s_branch .LBB0_129

.LBB0_138:
	s_or_b64 exec, exec, s[6:7]
	s_waitcnt vmcnt(0)
	s_waitcnt vmcnt(0)

.LBB0_156:
	s_or_b64 exec, exec, s[4:5]
	s_mov_b64 s[4:5], exec
	v_mbcnt_lo_u32_b32 v1, s4, 0
	v_mbcnt_hi_u32_b32 v1, s5, v1
	s_mov_b32 s9, 0
	v_cmp_eq_u32_e32 vcc, 0, v1
	s_waitcnt vmcnt(0)
	s_and_saveexec_b64 s[6:7], vcc
	s_cbranch_execz .LBB0_158
	s_add_i32 s8, s3, 0x900
	s_lshl_b64 s[8:9], s[8:9], 2
	s_add_u32 s8, s54, s8
	s_addc_u32 s9, s55, s9
	s_bcnt1_i32_b64 s3, s[4:5]
	v_mov_b32_e32 v1, 0
	v_mov_b32_e32 v2, s3

.LBB0_224:
	s_or_b64 exec, exec, s[6:7]
	v_cvt_f32_u32_e32 v6, v4
	s_waitcnt vmcnt(0)
	buffer_inv sc1
	v_readfirstlane_b32 s4, v5
	v_sub_u32_e32 v5, 0, v4
	v_rcp_iflag_f32_e32 v6, v6
	v_add_u32_e32 v7, s4, v3
	v_mul_f32_e32 v6, 0x4f7ffffe, v6
	v_cvt_u32_f32_e32 v6, v6
	v_mul_lo_u32 v3, v5, v6
	v_mul_hi_u32 v3, v6, v3
	v_add_u32_e32 v3, v6, v3
	v_mul_hi_u32 v3, v7, v3
	v_mul_lo_u32 v5, v3, v4
	v_sub_u32_e32 v5, v7, v5
	v_add_u32_e32 v6, 1, v3
	v_cmp_ge_u32_e32 vcc, v5, v4
	s_nop 1
	v_cndmask_b32_e32 v3, v3, v6, vcc
	v_sub_u32_e32 v6, v5, v4
	v_cndmask_b32_e32 v5, v5, v6, vcc
	v_add_u32_e32 v6, 1, v3
	v_cmp_ge_u32_e32 vcc, v5, v4
	v_add_u32_e32 v5, 1, v7
	s_nop 0
	v_cndmask_b32_e32 v3, v3, v6, vcc
	v_mul_lo_u32 v6, v4, v3
	v_add_u32_e32 v4, v6, v4
	v_cmp_ne_u32_e32 vcc, v5, v4
	s_and_saveexec_b64 s[4:5], vcc
	s_xor_b64 s[4:5], exec, s[4:5]
	s_cbranch_execz .LBB0_238
	s_movk_i32 s6, 0xd40
	s_mov_b32 s7, s56
	s_lshl_b64 s[6:7], s[6:7], 2
	s_add_u32 s8, s54, s6
	s_addc_u32 s9, s55, s7
	s_waitcnt lgkmcnt(0)
	global_load_dword v2, v227, s[8:9] sc1
	s_waitcnt vmcnt(0)
	v_cmp_eq_u32_e32 vcc, v2, v3
	s_and_saveexec_b64 s[6:7], vcc
	s_cbranch_execz .LBB0_237
	s_mov_b32 s21, 1
	s_mov_b64 s[10:11], 0
	s_branch .LBB0_228

.LBB0_255:
	s_or_b64 exec, exec, s[4:5]
	s_mov_b64 s[4:5], exec
	v_mbcnt_lo_u32_b32 v2, s4, 0
	v_mbcnt_hi_u32_b32 v2, s5, v2
	v_cmp_eq_u32_e32 vcc, 0, v2
	s_waitcnt vmcnt(0)
	s_and_saveexec_b64 s[6:7], vcc
	s_cbranch_execz .LBB0_257
	s_add_i32 s8, s20, 0x900
	s_mov_b32 s9, s56
	s_lshl_b64 s[8:9], s[8:9], 2
	s_add_u32 s8, s54, s8
	s_addc_u32 s9, s55, s9
	s_bcnt1_i32_b64 s4, s[4:5]
	v_mov_b32_e32 v2, s4

.LBB0_1381:
	s_or_b64 exec, exec, s[4:5]
	s_mov_b64 s[4:5], exec
	v_mbcnt_lo_u32_b32 v2, s4, 0
	v_mbcnt_hi_u32_b32 v2, s5, v2
	v_cmp_eq_u32_e32 vcc, 0, v2
	s_waitcnt vmcnt(0)
	s_and_saveexec_b64 s[6:7], vcc
	s_cbranch_execnz .LBB0_1382
	s_getpc_b64 s[98:99]
